# baseline (speedup 1.0000x reference)
.LBB1_18:
	v_lshl_add_u32 v32, v83, 4, v1
	v_lshl_add_u32 v33, v84, 5, v32
	ds_read_b128 v[2:5], v33 offset:28672
	ds_read_b128 v[6:9], v33 offset:28688
	s_waitcnt vmcnt(0)
	v_and_b32_e32 v42, 0xffff, v43
	v_mov_b32_e32 v43, 0
	v_mov_b32_e32 v44, v43
	s_waitcnt lgkmcnt(1)
	v_cvt_pk_f16_f32 v5, v4, v5
	s_waitcnt lgkmcnt(0)
	v_cndmask_b32_e64 v9, 1.0, v9, s[0:1]
	v_cvt_pk_f16_f32 v6, v6, v7
	v_cvt_pk_f16_f32 v4, v2, v3
	v_cvt_pk_f16_f32 v7, v8, v9
	v_mov_b32_e32 v45, v43
	v_and_b32_e32 v22, 0xffff, v47
	v_mov_b32_e32 v23, v43
	v_mov_b32_e32 v24, v43
	v_mov_b32_e32 v25, v43
	v_mfma_f32_32x32x16_f16 v[2:17], v[18:21], v[4:7], 0
	s_nop 15
	s_nop 3
	s_mov_b32 s2, 0x7fff7fff
	s_mov_b32 s3, 0xa714a714
	v_mov_b32_e32 v85, 0xb7d0b7d0
	s_mov_b32 s4, 0xbc90bc90
	v_cvt_pk_f16_f32 v30, v2, v3
	v_cvt_pk_f16_f32 v31, v4, v5
	v_and_b32 v28, s2, v30
	v_and_b32 v29, s2, v31
	v_pk_fma_f16 v26, v28, s3, v85
	v_pk_fma_f16 v27, v29, s3, v85
	v_pk_fma_f16 v26, v26, v28, s4
	v_pk_fma_f16 v27, v27, v29, s4
	v_lshl_add_u32 v47, v84, 3, v32
	v_pk_mul_f16 v26, v26, v28
	v_pk_mul_f16 v27, v27, v29
	v_exp_f16_sdwa v26, v26 dst_sel:WORD_0 dst_unused:UNUSED_PRESERVE src0_sel:WORD_0
	v_exp_f16_sdwa v27, v27 dst_sel:WORD_0 dst_unused:UNUSED_PRESERVE src0_sel:WORD_0
	v_exp_f16_sdwa v26, v26 dst_sel:WORD_1 dst_unused:UNUSED_PRESERVE src0_sel:WORD_1
	v_exp_f16_sdwa v27, v27 dst_sel:WORD_1 dst_unused:UNUSED_PRESERVE src0_sel:WORD_1
	v_pk_add_f16 v2, v30, v28
	v_pk_add_f16 v3, v31, v29
	v_pk_fma_f16 v26, v28, v26, v2 neg_lo:[1,0,0] neg_hi:[1,0,0]
	v_pk_fma_f16 v27, v29, v27, v3 neg_lo:[1,0,0] neg_hi:[1,0,0]
	s_nop 0
	v_cvt_pk_f16_f32 v4, v6, v7
	v_cvt_pk_f16_f32 v5, v8, v9
	v_and_b32 v2, s2, v4
	v_and_b32 v3, s2, v5
	v_pk_fma_f16 v28, v2, s3, v85
	v_pk_fma_f16 v29, v3, s3, v85
	v_pk_fma_f16 v28, v28, v2, s4
	v_pk_fma_f16 v29, v29, v3, s4
	s_nop 0
	v_pk_mul_f16 v28, v28, v2
	v_pk_mul_f16 v29, v29, v3
	v_exp_f16_sdwa v28, v28 dst_sel:WORD_0 dst_unused:UNUSED_PRESERVE src0_sel:WORD_0
	v_exp_f16_sdwa v29, v29 dst_sel:WORD_0 dst_unused:UNUSED_PRESERVE src0_sel:WORD_0
	v_exp_f16_sdwa v28, v28 dst_sel:WORD_1 dst_unused:UNUSED_PRESERVE src0_sel:WORD_1
	v_exp_f16_sdwa v29, v29 dst_sel:WORD_1 dst_unused:UNUSED_PRESERVE src0_sel:WORD_1
	v_pk_add_f16 v6, v4, v2
	v_pk_add_f16 v7, v5, v3
	v_pk_fma_f16 v28, v2, v28, v6 neg_lo:[1,0,0] neg_hi:[1,0,0]
	v_pk_fma_f16 v29, v3, v29, v7 neg_lo:[1,0,0] neg_hi:[1,0,0]
	v_cvt_pk_f16_f32 v4, v10, v11
	v_cvt_pk_f16_f32 v5, v12, v13
	v_and_b32 v2, s2, v4
	v_and_b32 v3, s2, v5
	v_pk_fma_f16 v30, v2, s3, v85
	v_pk_fma_f16 v31, v3, s3, v85
	v_pk_fma_f16 v30, v30, v2, s4
	v_pk_fma_f16 v31, v31, v3, s4
	s_nop 4
	v_add_u32_e32 v12, 0x7000, v47
	v_pk_mul_f16 v30, v30, v2
	v_pk_mul_f16 v31, v31, v3
	v_exp_f16_sdwa v30, v30 dst_sel:WORD_0 dst_unused:UNUSED_PRESERVE src0_sel:WORD_0
	v_exp_f16_sdwa v31, v31 dst_sel:WORD_0 dst_unused:UNUSED_PRESERVE src0_sel:WORD_0
	v_exp_f16_sdwa v30, v30 dst_sel:WORD_1 dst_unused:UNUSED_PRESERVE src0_sel:WORD_1
	v_exp_f16_sdwa v31, v31 dst_sel:WORD_1 dst_unused:UNUSED_PRESERVE src0_sel:WORD_1
	v_pk_add_f16 v6, v4, v2
	v_pk_add_f16 v7, v5, v3
	v_pk_fma_f16 v30, v2, v30, v6 neg_lo:[1,0,0] neg_hi:[1,0,0]
	v_pk_fma_f16 v31, v3, v31, v7 neg_lo:[1,0,0] neg_hi:[1,0,0]
	v_cvt_pk_f16_f32 v4, v14, v15
	v_cvt_pk_f16_f32 v5, v16, v17
	v_and_b32 v2, s2, v4
	v_and_b32 v3, s2, v5
	v_pk_fma_f16 v10, v2, s3, v85
	v_pk_fma_f16 v11, v3, s3, v85
	v_pk_fma_f16 v10, v10, v2, s4
	v_pk_fma_f16 v11, v11, v3, s4
	s_nop 0
	v_pk_mul_f16 v10, v10, v2
	v_pk_mul_f16 v11, v11, v3
	v_exp_f16_sdwa v10, v10 dst_sel:WORD_0 dst_unused:UNUSED_PRESERVE src0_sel:WORD_0
	v_exp_f16_sdwa v11, v11 dst_sel:WORD_0 dst_unused:UNUSED_PRESERVE src0_sel:WORD_0
	v_exp_f16_sdwa v10, v10 dst_sel:WORD_1 dst_unused:UNUSED_PRESERVE src0_sel:WORD_1
	v_exp_f16_sdwa v11, v11 dst_sel:WORD_1 dst_unused:UNUSED_PRESERVE src0_sel:WORD_1
	v_pk_add_f16 v6, v4, v2
	v_pk_add_f16 v7, v5, v3
	v_pk_fma_f16 v10, v2, v10, v6 neg_lo:[1,0,0] neg_hi:[1,0,0]
	v_pk_fma_f16 v11, v3, v11, v7 neg_lo:[1,0,0] neg_hi:[1,0,0]
	ds_read_b128 v[2:5], v33 offset:29248
	ds_read_b128 v[6:9], v33 offset:29264
	ds_write2_b64 v12, v[26:27], v[28:29] offset0:150 offset1:230
	v_add_u32_e32 v12, 0x7800, v47
	ds_write2_b64 v12, v[30:31], v[10:11] offset0:54 offset1:134
	s_waitcnt lgkmcnt(3)
	v_cvt_pk_f16_f32 v5, v4, v5
	s_waitcnt lgkmcnt(2)
	v_cndmask_b32_e64 v9, 1.0, v9, s[0:1]
	v_cvt_pk_f16_f32 v6, v6, v7
	v_cvt_pk_f16_f32 v4, v2, v3
	v_cvt_pk_f16_f32 v7, v8, v9
	s_nop 1
	v_mfma_f32_32x32x16_f16 v[2:17], v[18:21], v[4:7], 0
	s_nop 15
	s_nop 3
	v_cvt_pk_f16_f32 v20, v2, v3
	v_cvt_pk_f16_f32 v21, v4, v5
	v_and_b32 v18, s2, v20
	v_and_b32 v19, s2, v21
	v_pk_fma_f16 v48, v18, s3, v85
	v_pk_fma_f16 v49, v19, s3, v85
	v_pk_fma_f16 v48, v48, v18, s4
	v_pk_fma_f16 v49, v49, v19, s4
	s_movk_i32 s5, 0xa00
	v_pk_mul_f16 v48, v48, v18
	v_pk_mul_f16 v49, v49, v19
	v_exp_f16_sdwa v48, v48 dst_sel:WORD_0 dst_unused:UNUSED_PRESERVE src0_sel:WORD_0
	v_exp_f16_sdwa v49, v49 dst_sel:WORD_0 dst_unused:UNUSED_PRESERVE src0_sel:WORD_0
	v_exp_f16_sdwa v48, v48 dst_sel:WORD_1 dst_unused:UNUSED_PRESERVE src0_sel:WORD_1
	v_exp_f16_sdwa v49, v49 dst_sel:WORD_1 dst_unused:UNUSED_PRESERVE src0_sel:WORD_1
	v_pk_add_f16 v2, v20, v18
	v_pk_add_f16 v3, v21, v19
	v_pk_fma_f16 v48, v18, v48, v2 neg_lo:[1,0,0] neg_hi:[1,0,0]
	v_pk_fma_f16 v49, v19, v49, v3 neg_lo:[1,0,0] neg_hi:[1,0,0]
	v_lshlrev_b32_e32 v0, 5, v0
	v_cvt_pk_f16_f32 v18, v6, v7
	v_cvt_pk_f16_f32 v19, v8, v9
	v_and_b32 v4, s2, v18
	v_and_b32 v5, s2, v19
	v_pk_fma_f16 v2, v4, s3, v85
	v_pk_fma_f16 v3, v5, s3, v85
	v_pk_fma_f16 v2, v2, v4, s4
	v_pk_fma_f16 v3, v3, v5, s4
	v_and_b32_e32 v0, 0x1e0, v0
	v_pk_mul_f16 v2, v2, v4
	v_pk_mul_f16 v3, v3, v5
	v_exp_f16_sdwa v2, v2 dst_sel:WORD_0 dst_unused:UNUSED_PRESERVE src0_sel:WORD_0
	v_exp_f16_sdwa v3, v3 dst_sel:WORD_0 dst_unused:UNUSED_PRESERVE src0_sel:WORD_0
	v_exp_f16_sdwa v2, v2 dst_sel:WORD_1 dst_unused:UNUSED_PRESERVE src0_sel:WORD_1
	v_exp_f16_sdwa v3, v3 dst_sel:WORD_1 dst_unused:UNUSED_PRESERVE src0_sel:WORD_1
	v_pk_add_f16 v6, v18, v4
	v_pk_add_f16 v7, v19, v5
	v_pk_fma_f16 v2, v4, v2, v6 neg_lo:[1,0,0] neg_hi:[1,0,0]
	v_pk_fma_f16 v3, v5, v3, v7 neg_lo:[1,0,0] neg_hi:[1,0,0]
	v_mfma_f32_32x32x16_f16 v[18:33], v[22:25], v[38:41], 0
	v_cvt_pk_f16_f32 v8, v10, v11
	v_cvt_pk_f16_f32 v9, v12, v13
	v_and_b32 v6, s2, v8
	v_and_b32 v7, s2, v9
	v_pk_fma_f16 v4, v6, s3, v85
	v_pk_fma_f16 v5, v7, s3, v85
	v_pk_fma_f16 v4, v4, v6, s4
	v_pk_fma_f16 v5, v5, v7, s4
	s_nop 0
	v_pk_mul_f16 v4, v4, v6
	v_pk_mul_f16 v5, v5, v7
	v_exp_f16_sdwa v4, v4 dst_sel:WORD_0 dst_unused:UNUSED_PRESERVE src0_sel:WORD_0
	v_exp_f16_sdwa v5, v5 dst_sel:WORD_0 dst_unused:UNUSED_PRESERVE src0_sel:WORD_0
	v_exp_f16_sdwa v4, v4 dst_sel:WORD_1 dst_unused:UNUSED_PRESERVE src0_sel:WORD_1
	v_exp_f16_sdwa v5, v5 dst_sel:WORD_1 dst_unused:UNUSED_PRESERVE src0_sel:WORD_1
	v_pk_add_f16 v10, v8, v6
	v_pk_add_f16 v11, v9, v7
	v_pk_fma_f16 v4, v6, v4, v10 neg_lo:[1,0,0] neg_hi:[1,0,0]
	v_pk_fma_f16 v5, v7, v5, v11 neg_lo:[1,0,0] neg_hi:[1,0,0]
	s_nop 0
	v_cvt_pk_f16_f32 v10, v14, v15
	v_cvt_pk_f16_f32 v11, v16, v17
	v_and_b32 v8, s2, v10
	v_and_b32 v9, s2, v11
	v_pk_fma_f16 v6, v8, s3, v85
	v_pk_fma_f16 v7, v9, s3, v85
	v_pk_fma_f16 v6, v6, v8, s4
	v_pk_fma_f16 v7, v7, v9, s4
	s_nop 0
	v_pk_mul_f16 v6, v6, v8
	v_pk_mul_f16 v7, v7, v9
	v_exp_f16_sdwa v6, v6 dst_sel:WORD_0 dst_unused:UNUSED_PRESERVE src0_sel:WORD_0
	v_exp_f16_sdwa v7, v7 dst_sel:WORD_0 dst_unused:UNUSED_PRESERVE src0_sel:WORD_0
	v_exp_f16_sdwa v6, v6 dst_sel:WORD_1 dst_unused:UNUSED_PRESERVE src0_sel:WORD_1
	v_exp_f16_sdwa v7, v7 dst_sel:WORD_1 dst_unused:UNUSED_PRESERVE src0_sel:WORD_1
	v_pk_add_f16 v12, v10, v8
	v_pk_add_f16 v13, v11, v9
	v_pk_fma_f16 v6, v8, v6, v12 neg_lo:[1,0,0] neg_hi:[1,0,0]
	v_pk_fma_f16 v7, v9, v7, v13 neg_lo:[1,0,0] neg_hi:[1,0,0]
	s_nop 4
	v_add_u32_e32 v8, 0x7c00, v47
	ds_write2_b64 v8, v[48:49], v[2:3] offset0:86 offset1:166
	v_add_u32_e32 v2, 0x8000, v47
	ds_write2_b64 v2, v[4:5], v[6:7] offset0:118 offset1:198
	v_mfma_f32_32x32x16_f16 v[2:17], v[42:45], v[38:41], 0
	v_lshrrev_b32_e32 v38, 4, v83
	v_mad_u32_u24 v1, v38, s5, v1
	ds_read_b128 v[38:41], v46
	v_mul_u32_u24_e32 v42, 0x280, v84
	v_add3_u32 v0, v1, v42, v0
	ds_read_b128 v[42:45], v0 offset:29824
	ds_read_b128 v[78:81], v0 offset:29840
	ds_read_b128 v[86:89], v46 offset:1024
	s_waitcnt lgkmcnt(2)
	v_mfma_f32_32x32x16_f16 v[18:33], v[38:41], v[42:45], v[18:33]
	s_waitcnt lgkmcnt(0)
	v_mfma_f32_32x32x16_f16 v[2:17], v[86:89], v[42:45], v[2:17]
	ds_read_b128 v[38:41], v46 offset:2048
	ds_read_b128 v[42:45], v0 offset:31104
	ds_read_b128 v[86:89], v46 offset:3072
	ds_read_b128 v[90:93], v0 offset:29920
	s_waitcnt lgkmcnt(2)
	v_mfma_f32_32x32x16_f16 v[18:33], v[38:41], v[42:45], v[18:33]
	s_waitcnt lgkmcnt(1)
	v_mfma_f32_32x32x16_f16 v[2:17], v[86:89], v[42:45], v[2:17]
	ds_read_b128 v[38:41], v46 offset:4096
	ds_read_b128 v[42:45], v46 offset:5120
	s_waitcnt lgkmcnt(1)
	v_mfma_f32_32x32x16_f16 v[18:33], v[38:41], v[78:81], v[18:33]
	s_waitcnt lgkmcnt(0)
	v_mfma_f32_32x32x16_f16 v[2:17], v[42:45], v[78:81], v[2:17]
	ds_read_b128 v[38:41], v46 offset:6144
	ds_read_b128 v[42:45], v0 offset:31120
	ds_read_b128 v[78:81], v46 offset:7168
	ds_read_b128 v[86:89], v0 offset:31136
	s_waitcnt lgkmcnt(2)
	v_mfma_f32_32x32x16_f16 v[18:33], v[38:41], v[42:45], v[18:33]
	s_waitcnt lgkmcnt(1)
	v_mfma_f32_32x32x16_f16 v[2:17], v[78:81], v[42:45], v[2:17]
	ds_read_b128 v[38:41], v46 offset:8192
	ds_read_b128 v[42:45], v0 offset:29856
	ds_read_b128 v[78:81], v0 offset:29872
	ds_read_b128 v[94:97], v46 offset:9216
	s_waitcnt lgkmcnt(2)
	v_mfma_f32_32x32x16_f16 v[18:33], v[38:41], v[42:45], v[18:33]
	s_waitcnt lgkmcnt(0)
	v_mfma_f32_32x32x16_f16 v[2:17], v[94:97], v[42:45], v[2:17]
	ds_read_b128 v[38:41], v46 offset:10240
	ds_read_b128 v[42:45], v46 offset:11264
	s_waitcnt lgkmcnt(1)
	v_mfma_f32_32x32x16_f16 v[18:33], v[38:41], v[86:89], v[18:33]
	s_waitcnt lgkmcnt(0)
	v_mfma_f32_32x32x16_f16 v[2:17], v[42:45], v[86:89], v[2:17]
	ds_read_b128 v[38:41], v46 offset:12288
	ds_read_b128 v[42:45], v46 offset:13312
	s_waitcnt lgkmcnt(1)
	v_mfma_f32_32x32x16_f16 v[18:33], v[38:41], v[78:81], v[18:33]
	s_waitcnt lgkmcnt(0)
	v_mfma_f32_32x32x16_f16 v[2:17], v[42:45], v[78:81], v[2:17]
	ds_read_b128 v[38:41], v46 offset:14336
	ds_read_b128 v[42:45], v0 offset:31152
	ds_read_b128 v[78:81], v46 offset:15360
	ds_read_b128 v[86:89], v0 offset:31168
	s_waitcnt lgkmcnt(2)
	v_mfma_f32_32x32x16_f16 v[18:33], v[38:41], v[42:45], v[18:33]
	s_waitcnt lgkmcnt(1)
	v_mfma_f32_32x32x16_f16 v[2:17], v[78:81], v[42:45], v[2:17]
	ds_read_b128 v[38:41], v46 offset:16384
	ds_read_b128 v[42:45], v0 offset:29888
	ds_read_b128 v[78:81], v46 offset:17408
	ds_read_b128 v[94:97], v0 offset:29904
	s_waitcnt lgkmcnt(2)
	v_mfma_f32_32x32x16_f16 v[18:33], v[38:41], v[42:45], v[18:33]
	s_waitcnt lgkmcnt(1)
	v_mfma_f32_32x32x16_f16 v[2:17], v[78:81], v[42:45], v[2:17]
	ds_read_b128 v[38:41], v46 offset:18432
	ds_read_b128 v[42:45], v46 offset:19456
	s_waitcnt lgkmcnt(1)
	v_mfma_f32_32x32x16_f16 v[18:33], v[38:41], v[86:89], v[18:33]
	s_waitcnt lgkmcnt(0)
	v_mfma_f32_32x32x16_f16 v[2:17], v[42:45], v[86:89], v[2:17]
	ds_read_b128 v[38:41], v46 offset:20480
	ds_read_b128 v[42:45], v46 offset:21504
	s_waitcnt lgkmcnt(1)
	v_mfma_f32_32x32x16_f16 v[18:33], v[38:41], v[94:97], v[18:33]
	s_waitcnt lgkmcnt(0)
	v_mfma_f32_32x32x16_f16 v[2:17], v[42:45], v[94:97], v[2:17]
	ds_read_b128 v[38:41], v46 offset:22528
	ds_read_b128 v[42:45], v0 offset:31184
	ds_read_b128 v[78:81], v46 offset:23552
	ds_read_b128 v[86:89], v0 offset:31200
	s_waitcnt lgkmcnt(2)
	v_mfma_f32_32x32x16_f16 v[18:33], v[38:41], v[42:45], v[18:33]
	s_waitcnt lgkmcnt(1)
	v_mfma_f32_32x32x16_f16 v[2:17], v[78:81], v[42:45], v[2:17]
	ds_read_b128 v[38:41], v46 offset:24576
	ds_read_b128 v[42:45], v46 offset:25600
	s_waitcnt lgkmcnt(1)
	v_mfma_f32_32x32x16_f16 v[18:33], v[38:41], v[90:93], v[18:33]
	s_waitcnt lgkmcnt(0)
	v_mfma_f32_32x32x16_f16 v[2:17], v[42:45], v[90:93], v[2:17]
	ds_read_b128 v[38:41], v46 offset:26624
	ds_read_b128 v[42:45], v46 offset:27648
	s_waitcnt lgkmcnt(1)
	v_mfma_f32_32x32x16_f16 v[18:33], v[38:41], v[86:89], v[18:33]
	s_waitcnt lgkmcnt(0)
	v_mfma_f32_32x32x16_f16 v[2:17], v[42:45], v[86:89], v[2:17]
	s_nop 15
	s_nop 3
	v_cvt_pk_f16_f32 v38, v18, v19
	v_cvt_pk_f16_f32 v39, v20, v21
	v_and_b32 v0, s2, v38
	v_and_b32 v1, s2, v39
	v_pk_fma_f16 v78, v0, s3, v85
	v_pk_fma_f16 v79, v1, s3, v85
	v_pk_fma_f16 v78, v78, v0, s4
	v_pk_fma_f16 v79, v79, v1, s4
	s_mov_b32 s5, 0xbf9353fd
	v_pk_mul_f16 v78, v78, v0
	v_pk_mul_f16 v79, v79, v1
	v_exp_f16_sdwa v78, v78 dst_sel:WORD_0 dst_unused:UNUSED_PRESERVE src0_sel:WORD_0
	v_exp_f16_sdwa v79, v79 dst_sel:WORD_0 dst_unused:UNUSED_PRESERVE src0_sel:WORD_0
	v_exp_f16_sdwa v78, v78 dst_sel:WORD_1 dst_unused:UNUSED_PRESERVE src0_sel:WORD_1
	v_exp_f16_sdwa v79, v79 dst_sel:WORD_1 dst_unused:UNUSED_PRESERVE src0_sel:WORD_1
	v_pk_add_f16 v18, v38, v0
	v_pk_add_f16 v19, v39, v1
	v_pk_fma_f16 v78, v0, v78, v18 neg_lo:[1,0,0] neg_hi:[1,0,0]
	v_pk_fma_f16 v79, v1, v79, v19 neg_lo:[1,0,0] neg_hi:[1,0,0]
	s_nop 0
	v_cvt_pk_f16_f32 v18, v22, v23
	v_cvt_pk_f16_f32 v19, v24, v25
	v_and_b32 v0, s2, v18
	v_and_b32 v1, s2, v19
	v_pk_fma_f16 v80, v0, s3, v85
	v_pk_fma_f16 v81, v1, s3, v85
	v_pk_fma_f16 v80, v80, v0, s4
	v_pk_fma_f16 v81, v81, v1, s4
	s_nop 0
	v_pk_mul_f16 v80, v80, v0
	v_pk_mul_f16 v81, v81, v1
	v_exp_f16_sdwa v80, v80 dst_sel:WORD_0 dst_unused:UNUSED_PRESERVE src0_sel:WORD_0
	v_exp_f16_sdwa v81, v81 dst_sel:WORD_0 dst_unused:UNUSED_PRESERVE src0_sel:WORD_0
	v_exp_f16_sdwa v80, v80 dst_sel:WORD_1 dst_unused:UNUSED_PRESERVE src0_sel:WORD_1
	v_exp_f16_sdwa v81, v81 dst_sel:WORD_1 dst_unused:UNUSED_PRESERVE src0_sel:WORD_1
	v_pk_add_f16 v20, v18, v0
	v_pk_add_f16 v21, v19, v1
	v_pk_fma_f16 v80, v0, v80, v20 neg_lo:[1,0,0] neg_hi:[1,0,0]
	v_pk_fma_f16 v81, v1, v81, v21 neg_lo:[1,0,0] neg_hi:[1,0,0]
	v_cvt_pk_f16_f32 v22, v26, v27
	v_cvt_pk_f16_f32 v23, v28, v29
	v_and_b32 v0, s2, v22
	v_and_b32 v1, s2, v23
	v_pk_fma_f16 v18, v0, s3, v85
	v_pk_fma_f16 v19, v1, s3, v85
	v_pk_fma_f16 v18, v18, v0, s4
	v_pk_fma_f16 v19, v19, v1, s4
	s_nop 0
	v_cvt_pk_f16_f32 v26, v30, v31
	v_cvt_pk_f16_f32 v27, v32, v33
	v_and_b32 v24, s2, v26
	v_and_b32 v25, s2, v27
	v_pk_fma_f16 v20, v24, s3, v85
	v_pk_fma_f16 v21, v25, s3, v85
	v_pk_fma_f16 v20, v20, v24, s4
	v_pk_fma_f16 v21, v21, v25, s4
	s_nop 5
	v_lshlrev_b32_e32 v30, 2, v83
	global_load_dword v31, v30, s[10:11]
	global_load_dword v32, v30, s[26:27]
	global_load_dword v33, v30, s[10:11] offset:128
	v_pk_mul_f16 v18, v18, v0
	v_pk_mul_f16 v19, v19, v1
	v_exp_f16_sdwa v18, v18 dst_sel:WORD_0 dst_unused:UNUSED_PRESERVE src0_sel:WORD_0
	v_exp_f16_sdwa v19, v19 dst_sel:WORD_0 dst_unused:UNUSED_PRESERVE src0_sel:WORD_0
	v_exp_f16_sdwa v18, v18 dst_sel:WORD_1 dst_unused:UNUSED_PRESERVE src0_sel:WORD_1
	v_exp_f16_sdwa v19, v19 dst_sel:WORD_1 dst_unused:UNUSED_PRESERVE src0_sel:WORD_1
	v_pk_add_f16 v28, v22, v0
	v_pk_add_f16 v29, v23, v1
	v_pk_fma_f16 v18, v0, v18, v28 neg_lo:[1,0,0] neg_hi:[1,0,0]
	v_pk_fma_f16 v19, v1, v19, v29 neg_lo:[1,0,0] neg_hi:[1,0,0]
	global_load_dword v30, v30, s[26:27] offset:128
	v_pk_mul_f16 v20, v20, v24
	v_pk_mul_f16 v21, v21, v25
	v_exp_f16_sdwa v20, v20 dst_sel:WORD_0 dst_unused:UNUSED_PRESERVE src0_sel:WORD_0
	v_exp_f16_sdwa v21, v21 dst_sel:WORD_0 dst_unused:UNUSED_PRESERVE src0_sel:WORD_0
	v_exp_f16_sdwa v20, v20 dst_sel:WORD_1 dst_unused:UNUSED_PRESERVE src0_sel:WORD_1
	v_exp_f16_sdwa v21, v21 dst_sel:WORD_1 dst_unused:UNUSED_PRESERVE src0_sel:WORD_1
	v_pk_add_f16 v0, v26, v24
	v_pk_add_f16 v1, v27, v25
	v_pk_fma_f16 v20, v24, v20, v0 neg_lo:[1,0,0] neg_hi:[1,0,0]
	v_pk_fma_f16 v21, v25, v21, v1 neg_lo:[1,0,0] neg_hi:[1,0,0]
	v_mfma_f32_32x32x16_f16 v[34:49], v[78:81], v[34:37], 0
	v_cvt_pk_f16_f32 v26, v2, v3
	v_cvt_pk_f16_f32 v27, v4, v5
	v_and_b32 v0, s2, v26
	v_and_b32 v1, s2, v27
	v_pk_fma_f16 v22, v0, s3, v85
	v_pk_fma_f16 v23, v1, s3, v85
	v_pk_fma_f16 v22, v22, v0, s4
	v_pk_fma_f16 v23, v23, v1, s4
	v_cvt_pk_f16_f32 v4, v6, v7
	v_cvt_pk_f16_f32 v5, v8, v9
	v_and_b32 v2, s2, v4
	v_and_b32 v3, s2, v5
	v_pk_fma_f16 v24, v2, s3, v85
	v_pk_fma_f16 v25, v3, s3, v85
	v_pk_fma_f16 v24, v24, v2, s4
	v_pk_fma_f16 v25, v25, v3, s4
	s_nop 0
	v_pk_mul_f16 v22, v22, v0
	v_pk_mul_f16 v23, v23, v1
	v_exp_f16_sdwa v22, v22 dst_sel:WORD_0 dst_unused:UNUSED_PRESERVE src0_sel:WORD_0
	v_exp_f16_sdwa v23, v23 dst_sel:WORD_0 dst_unused:UNUSED_PRESERVE src0_sel:WORD_0
	v_exp_f16_sdwa v22, v22 dst_sel:WORD_1 dst_unused:UNUSED_PRESERVE src0_sel:WORD_1
	v_exp_f16_sdwa v23, v23 dst_sel:WORD_1 dst_unused:UNUSED_PRESERVE src0_sel:WORD_1
	v_pk_add_f16 v6, v26, v0
	v_pk_add_f16 v7, v27, v1
	v_pk_fma_f16 v22, v0, v22, v6 neg_lo:[1,0,0] neg_hi:[1,0,0]
	v_pk_fma_f16 v23, v1, v23, v7 neg_lo:[1,0,0] neg_hi:[1,0,0]
	v_pk_mul_f16 v24, v24, v2
	v_pk_mul_f16 v25, v25, v3
	v_exp_f16_sdwa v24, v24 dst_sel:WORD_0 dst_unused:UNUSED_PRESERVE src0_sel:WORD_0
	v_exp_f16_sdwa v25, v25 dst_sel:WORD_0 dst_unused:UNUSED_PRESERVE src0_sel:WORD_0
	v_exp_f16_sdwa v24, v24 dst_sel:WORD_1 dst_unused:UNUSED_PRESERVE src0_sel:WORD_1
	v_exp_f16_sdwa v25, v25 dst_sel:WORD_1 dst_unused:UNUSED_PRESERVE src0_sel:WORD_1
	v_pk_add_f16 v0, v4, v2
	v_pk_add_f16 v1, v5, v3
	v_pk_fma_f16 v24, v2, v24, v0 neg_lo:[1,0,0] neg_hi:[1,0,0]
	v_pk_fma_f16 v25, v3, v25, v1 neg_lo:[1,0,0] neg_hi:[1,0,0]
	s_nop 0
	v_cvt_pk_f16_f32 v2, v10, v11
	v_cvt_pk_f16_f32 v3, v12, v13
	v_and_b32 v0, s2, v2
	v_and_b32 v1, s2, v3
	v_pk_fma_f16 v26, v0, s3, v85
	v_pk_fma_f16 v27, v1, s3, v85
	v_pk_fma_f16 v26, v26, v0, s4
	v_pk_fma_f16 v27, v27, v1, s4
	v_cvt_pk_f16_f32 v6, v14, v15
	v_cvt_pk_f16_f32 v7, v16, v17
	v_and_b32 v4, s2, v6
	v_and_b32 v5, s2, v7
	v_pk_fma_f16 v28, v4, s3, v85
	v_pk_fma_f16 v29, v5, s3, v85
	v_pk_fma_f16 v28, v28, v4, s4
	v_pk_fma_f16 v29, v29, v5, s4
	v_mfma_f32_32x32x16_f16 v[34:49], v[18:21], v[74:77], v[34:49]
	v_pk_mul_f16 v26, v26, v0
	v_pk_mul_f16 v27, v27, v1
	v_exp_f16_sdwa v26, v26 dst_sel:WORD_0 dst_unused:UNUSED_PRESERVE src0_sel:WORD_0
	v_exp_f16_sdwa v27, v27 dst_sel:WORD_0 dst_unused:UNUSED_PRESERVE src0_sel:WORD_0
	v_exp_f16_sdwa v26, v26 dst_sel:WORD_1 dst_unused:UNUSED_PRESERVE src0_sel:WORD_1
	v_exp_f16_sdwa v27, v27 dst_sel:WORD_1 dst_unused:UNUSED_PRESERVE src0_sel:WORD_1
	v_pk_add_f16 v8, v2, v0
	v_pk_add_f16 v9, v3, v1
	v_pk_fma_f16 v26, v0, v26, v8 neg_lo:[1,0,0] neg_hi:[1,0,0]
	v_pk_fma_f16 v27, v1, v27, v9 neg_lo:[1,0,0] neg_hi:[1,0,0]
	v_pk_mul_f16 v28, v28, v4
	v_pk_mul_f16 v29, v29, v5
	v_exp_f16_sdwa v28, v28 dst_sel:WORD_0 dst_unused:UNUSED_PRESERVE src0_sel:WORD_0
	v_exp_f16_sdwa v29, v29 dst_sel:WORD_0 dst_unused:UNUSED_PRESERVE src0_sel:WORD_0
	v_exp_f16_sdwa v28, v28 dst_sel:WORD_1 dst_unused:UNUSED_PRESERVE src0_sel:WORD_1
	v_exp_f16_sdwa v29, v29 dst_sel:WORD_1 dst_unused:UNUSED_PRESERVE src0_sel:WORD_1
	v_pk_add_f16 v0, v6, v4
	v_pk_add_f16 v1, v7, v5
	v_pk_fma_f16 v28, v4, v28, v0 neg_lo:[1,0,0] neg_hi:[1,0,0]
	v_pk_fma_f16 v29, v5, v29, v1 neg_lo:[1,0,0] neg_hi:[1,0,0]
	s_lshl_b32 s2, s30, 12
	v_mbcnt_lo_u32_b32 v0, -1, 0
	v_mbcnt_hi_u32_b32 v0, -1, v0
	v_and_b32_e32 v2, 64, v0
	v_xor_b32_e32 v1, 32, v0
	v_add_u32_e32 v2, 64, v2
	v_cmp_lt_i32_e32 vcc, v1, v2
	v_mfma_f32_32x32x16_f16 v[34:49], v[22:25], v[70:73], v[34:49]
	s_mov_b32 s3, 0xbd5597ee
	v_cndmask_b32_e32 v16, v0, v1, vcc
	s_mov_b32 s4, 0xbeeb5020
	v_mfma_f32_32x32x16_f16 v[0:15], v[78:81], v[66:69], 0
	v_mfma_f32_32x32x16_f16 v[0:15], v[18:21], v[58:61], v[0:15]
	v_mfma_f32_32x32x16_f16 v[0:15], v[22:25], v[54:57], v[0:15]
	v_mov_b32_e32 v22, 0x3bebe41f
	v_mfma_f32_32x32x16_f16 v[34:49], v[26:29], v[62:65], v[34:49]
	v_lshlrev_b32_e32 v62, 2, v16
	v_lshl_add_u32 v16, v82, 1, s2
	s_mov_b32 s2, 0xb9ffea6a
	v_or_b32_e32 v16, v16, v84
	v_lshlrev_b32_e32 v63, 6, v16
	v_or_b32_e32 v16, v63, v83
	v_ashrrev_i32_e32 v17, 31, v16
	v_mfma_f32_32x32x16_f16 v[0:15], v[26:29], v[50:53], v[0:15]
	s_nop 3
	v_add_f32_e32 v34, v34, v35
	v_add_f32_e32 v18, v36, v37
	v_add_f32_e32 v19, v38, v39
	v_add_f32_e32 v20, v40, v41
	v_add_f32_e32 v21, v42, v43
	v_add_f32_e32 v35, v44, v45
	v_add_f32_e32 v36, v46, v47
	v_add_f32_e32 v37, v48, v49
	v_add_f32_e32 v0, v0, v1
	v_add_f32_e32 v1, v2, v3
	v_add_f32_e32 v2, v4, v5
	v_add_f32_e32 v3, v6, v7
	v_add_f32_e32 v4, v8, v9
	v_add_f32_e32 v5, v10, v11
	v_add_f32_e32 v8, v34, v18
	v_add_f32_e32 v9, v19, v20
	v_add_f32_e32 v10, v21, v35
	v_add_f32_e32 v11, v36, v37
	v_add_f32_e32 v0, v0, v1
	v_add_f32_e32 v1, v2, v3
	v_add_f32_e32 v2, v4, v5
	v_add_f32_e32 v3, v8, v9
	v_add_f32_e32 v4, v10, v11
	v_mov_b32_e32 v5, v3
	v_mov_b32_e32 v8, v4
	s_nop 1
	v_permlane32_swap_b32_e32 v3, v5
	v_permlane32_swap_b32_e32 v4, v8
	v_add_f32_e32 v6, v12, v13
	v_add_f32_e32 v7, v14, v15
	v_add_f32_e32 v6, v6, v7
	v_add_f32_e32 v0, v0, v1
	v_add_f32_e32 v1, v2, v6
	s_waitcnt lgkmcnt(1)
	v_add_f32_e32 v2, v3, v5
	s_waitcnt lgkmcnt(0)
	v_add_f32_e32 v3, v4, v8
	v_cndmask_b32_e64 v2, v3, v2, s[0:1]
	s_waitcnt vmcnt(3)
	v_add_f32_e32 v2, v31, v2
	v_fma_f32 v3, |v2|, s2, v22
	v_fma_f32 v3, v3, |v2|, s3
	v_fma_f32 v3, v3, |v2|, s4
	v_mov_b32_e32 v4, v0
	v_mov_b32_e32 v5, v1
	s_nop 1
	v_permlane32_swap_b32_e32 v0, v4
	v_permlane32_swap_b32_e32 v1, v5
	v_fma_f32 v3, v3, |v2|, s5
	v_fma_f32 v3, v3, |v2|, -1.0
	v_exp_f32_e32 v3, v3
	s_waitcnt lgkmcnt(1)
	v_add_f32_e32 v0, v0, v4
	s_waitcnt lgkmcnt(0)
	v_add_f32_e32 v1, v1, v5
	v_max_f32_e32 v6, 0, v2
	v_cndmask_b32_e64 v0, v1, v0, s[0:1]
	v_fma_f32 v2, -|v2|, v3, v6
	s_waitcnt vmcnt(1)
	v_add_f32_e32 v3, v33, v0
	v_fma_f32 v0, |v3|, s2, v22
	v_fma_f32 v0, v0, |v3|, s3
	v_fma_f32 v0, v0, |v3|, s4
	v_fma_f32 v0, v0, |v3|, s5
	v_fma_f32 v0, v0, |v3|, -1.0
	v_exp_f32_e32 v4, v0
	v_add_f32_e32 v2, v32, v2
	v_lshl_add_u64 v[0:1], v[16:17], 2, s[14:15]
	global_store_dword v[0:1], v2, off
	v_max_f32_e32 v0, 0, v3
	v_fma_f32 v0, -|v3|, v4, v0
	v_ashrrev_i32_e32 v17, 31, v63
	s_waitcnt vmcnt(1)
	v_add_f32_e32 v2, v30, v0
	v_lshl_add_u64 v[0:1], v[16:17], 2, s[14:15]
	global_store_dword v[0:1], v2, off offset:128
	s_endpgm
